# v55 + hand-written publish of the post-norm row statistics (out-proj, down): packed sum of squares, the eight partial sums cross lane halves in one LDS round trip instead of eight serialized ones
# baseline (speedup 1.0000x reference)
; #define PG8_LAS __attribute__((address_space(3)))
;     __device__ __forceinline__ void publish(const f32x4 (&v)[2][2][4][2], const Unit& u, int wr, int wc, int fr, int fq, PG8_LAS unsigned char* lds, int wid, int lane) const {
;         PG8_LAS float* P = (PG8_LAS float*)lds;
; #pragma unroll
;         for (int ai = 0; ai < 2; ++ai)
; #pragma unroll
;             for (int m = 0; m < 4; ++m) {
;                 float s = 0.f;
; #pragma unroll
;                 for (int bj = 0; bj < 2; ++bj)
; #pragma unroll
;                     for (int n = 0; n < 2; ++n) { const f32x4 x = v[ai][bj][m][n]; s += (x[0] * x[0] + x[1] * x[1]) + (x[2] * x[2] + x[3] * x[3]); }
;                 s = xor_add<16>(s); s = xor_add<32>(s);
;                 if (fq == 0) P[(ai * HALF + wr * 64 + m * 16 + fr) * 4 + wc] = s;
;             }
;         asm volatile("s_waitcnt lgkmcnt(0)" ::: "memory"); __builtin_amdgcn_s_barrier(); asm volatile("" ::: "memory");
;         const int row = wid * 32 + (lane & 31);
;         if (lane < 32) {
;             const float tot = (P[row * 4 + 0] + P[row * 4 + 1]) + (P[row * 4 + 2] + P[row * 4 + 3]);
;             __hip_atomic_store(xbuf + ((size_t)(u.pm * BM + row) * 4 + u.pn), __float_as_uint(tot) + 1u, __ATOMIC_RELAXED, __HIP_MEMORY_SCOPE_AGENT);
;         }
.LBB0_1307:
	v_and_b32_e32 v2, 63, v146
	s_lshl_b32 s0, s23, 2
	v_cmp_gt_u32_e64 s[4:5], 16, v2
	s_add_i32 s20, s0, 0
	s_lshl_b32 s6, s22, 10
	s_add_i32 s6, s20, s6
	v_lshl_add_u32 v134, v147, 4, s6
	v_pk_mul_f32 v[244:245], v[116:117], v[116:117]
	v_pk_mul_f32 v[246:247], v[100:101], v[100:101]
	v_pk_fma_f32 v[244:245], v[118:119], v[118:119], v[244:245]
	v_pk_fma_f32 v[246:247], v[102:103], v[102:103], v[246:247]
	v_pk_fma_f32 v[244:245], v[120:121], v[120:121], v[244:245]
	v_pk_fma_f32 v[246:247], v[104:105], v[104:105], v[246:247]
	v_pk_fma_f32 v[244:245], v[122:123], v[122:123], v[244:245]
	v_pk_fma_f32 v[246:247], v[106:107], v[106:107], v[246:247]
	v_pk_fma_f32 v[244:245], v[124:125], v[124:125], v[244:245]
	v_pk_fma_f32 v[246:247], v[108:109], v[108:109], v[246:247]
	v_pk_fma_f32 v[244:245], v[126:127], v[126:127], v[244:245]
	v_pk_fma_f32 v[246:247], v[110:111], v[110:111], v[246:247]
	v_pk_fma_f32 v[244:245], v[128:129], v[128:129], v[244:245]
	v_pk_fma_f32 v[246:247], v[112:113], v[112:113], v[246:247]
	v_pk_fma_f32 v[244:245], v[130:131], v[130:131], v[244:245]
	v_pk_fma_f32 v[246:247], v[114:115], v[114:115], v[246:247]
	v_add_f32_e32 v236, v244, v245
	v_add_f32_e32 v237, v246, v247
	v_pk_mul_f32 v[244:245], v[84:85], v[84:85]
	v_pk_mul_f32 v[246:247], v[68:69], v[68:69]
	v_pk_fma_f32 v[244:245], v[86:87], v[86:87], v[244:245]
	v_pk_fma_f32 v[246:247], v[70:71], v[70:71], v[246:247]
	v_pk_fma_f32 v[244:245], v[88:89], v[88:89], v[244:245]
	v_pk_fma_f32 v[246:247], v[72:73], v[72:73], v[246:247]
	v_pk_fma_f32 v[244:245], v[90:91], v[90:91], v[244:245]
	v_pk_fma_f32 v[246:247], v[74:75], v[74:75], v[246:247]
	v_pk_fma_f32 v[244:245], v[92:93], v[92:93], v[244:245]
	v_pk_fma_f32 v[246:247], v[76:77], v[76:77], v[246:247]
	v_pk_fma_f32 v[244:245], v[94:95], v[94:95], v[244:245]
	v_pk_fma_f32 v[246:247], v[78:79], v[78:79], v[246:247]
	v_pk_fma_f32 v[244:245], v[96:97], v[96:97], v[244:245]
	v_pk_fma_f32 v[246:247], v[80:81], v[80:81], v[246:247]
	v_pk_fma_f32 v[244:245], v[98:99], v[98:99], v[244:245]
	v_pk_fma_f32 v[246:247], v[82:83], v[82:83], v[246:247]
	v_add_f32_e32 v238, v244, v245
	v_add_f32_e32 v239, v246, v247
	v_pk_mul_f32 v[244:245], v[52:53], v[52:53]
	v_pk_mul_f32 v[246:247], v[36:37], v[36:37]
	v_pk_fma_f32 v[244:245], v[54:55], v[54:55], v[244:245]
	v_pk_fma_f32 v[246:247], v[38:39], v[38:39], v[246:247]
	v_pk_fma_f32 v[244:245], v[56:57], v[56:57], v[244:245]
	v_pk_fma_f32 v[246:247], v[40:41], v[40:41], v[246:247]
	v_pk_fma_f32 v[244:245], v[58:59], v[58:59], v[244:245]
	v_pk_fma_f32 v[246:247], v[42:43], v[42:43], v[246:247]
	v_pk_fma_f32 v[244:245], v[60:61], v[60:61], v[244:245]
	v_pk_fma_f32 v[246:247], v[44:45], v[44:45], v[246:247]
	v_pk_fma_f32 v[244:245], v[62:63], v[62:63], v[244:245]
	v_pk_fma_f32 v[246:247], v[46:47], v[46:47], v[246:247]
	v_pk_fma_f32 v[244:245], v[64:65], v[64:65], v[244:245]
	v_pk_fma_f32 v[246:247], v[48:49], v[48:49], v[246:247]
	v_pk_fma_f32 v[244:245], v[66:67], v[66:67], v[244:245]
	v_pk_fma_f32 v[246:247], v[50:51], v[50:51], v[246:247]
	v_add_f32_e32 v240, v244, v245
	v_add_f32_e32 v241, v246, v247
	v_pk_mul_f32 v[244:245], v[20:21], v[20:21]
	v_pk_mul_f32 v[246:247], v[4:5], v[4:5]
	v_pk_fma_f32 v[244:245], v[22:23], v[22:23], v[244:245]
	v_pk_fma_f32 v[246:247], v[6:7], v[6:7], v[246:247]
	v_pk_fma_f32 v[244:245], v[24:25], v[24:25], v[244:245]
	v_pk_fma_f32 v[246:247], v[8:9], v[8:9], v[246:247]
	v_pk_fma_f32 v[244:245], v[26:27], v[26:27], v[244:245]
	v_pk_fma_f32 v[246:247], v[10:11], v[10:11], v[246:247]
	v_pk_fma_f32 v[244:245], v[28:29], v[28:29], v[244:245]
	v_pk_fma_f32 v[246:247], v[12:13], v[12:13], v[246:247]
	v_pk_fma_f32 v[244:245], v[30:31], v[30:31], v[244:245]
	v_pk_fma_f32 v[246:247], v[14:15], v[14:15], v[246:247]
	v_pk_fma_f32 v[244:245], v[32:33], v[32:33], v[244:245]
	v_pk_fma_f32 v[246:247], v[16:17], v[16:17], v[246:247]
	v_pk_fma_f32 v[244:245], v[34:35], v[34:35], v[244:245]
	v_pk_fma_f32 v[246:247], v[18:19], v[18:19], v[246:247]
	v_add_f32_e32 v242, v244, v245
	v_add_f32_e32 v243, v246, v247
	ds_swizzle_b32 v244, v236 offset:swizzle(SWAP,16)
	ds_swizzle_b32 v245, v237 offset:swizzle(SWAP,16)
	ds_swizzle_b32 v246, v238 offset:swizzle(SWAP,16)
	ds_swizzle_b32 v247, v239 offset:swizzle(SWAP,16)
	ds_swizzle_b32 v248, v240 offset:swizzle(SWAP,16)
	ds_swizzle_b32 v249, v241 offset:swizzle(SWAP,16)
	ds_swizzle_b32 v250, v242 offset:swizzle(SWAP,16)
	ds_swizzle_b32 v251, v243 offset:swizzle(SWAP,16)
	s_waitcnt lgkmcnt(0)
	v_add_f32_e32 v236, v236, v244
	v_add_f32_e32 v237, v237, v245
	v_add_f32_e32 v238, v238, v246
	v_add_f32_e32 v239, v239, v247
	v_add_f32_e32 v240, v240, v248
	v_add_f32_e32 v241, v241, v249
	v_add_f32_e32 v242, v242, v250
	v_add_f32_e32 v243, v243, v251
	v_mov_b32_e32 v244, v236
	v_mov_b32_e32 v245, v237
	v_mov_b32_e32 v246, v238
	v_mov_b32_e32 v247, v239
	v_mov_b32_e32 v248, v240
	v_mov_b32_e32 v249, v241
	v_mov_b32_e32 v250, v242
	v_mov_b32_e32 v251, v243
	s_nop 1
	v_permlane32_swap_b32_e32 v236, v244
	v_permlane32_swap_b32_e32 v237, v245
	v_permlane32_swap_b32_e32 v238, v246
	v_permlane32_swap_b32_e32 v239, v247
	v_permlane32_swap_b32_e32 v240, v248
	v_permlane32_swap_b32_e32 v241, v249
	v_permlane32_swap_b32_e32 v242, v250
	v_permlane32_swap_b32_e32 v243, v251
	s_barrier
	s_and_saveexec_b64 s[0:1], s[4:5]
	v_add_f32_e32 v236, v236, v244
	v_add_f32_e32 v237, v237, v245
	v_add_f32_e32 v238, v238, v246
	v_add_f32_e32 v239, v239, v247
	v_add_f32_e32 v240, v240, v248
	v_add_f32_e32 v241, v241, v249
	v_add_f32_e32 v242, v242, v250
	v_add_f32_e32 v243, v243, v251
	ds_write_b32 v134, v236
	ds_write_b32 v134, v237 offset:256
	ds_write_b32 v134, v238 offset:512
	ds_write_b32 v134, v239 offset:768
	ds_write_b32 v134, v240 offset:2048
	ds_write_b32 v134, v241 offset:2304
	ds_write_b32 v134, v242 offset:2560
	ds_write_b32 v134, v243 offset:2816
	s_or_b64 exec, exec, s[0:1]
	s_lshl_b32 s0, s77, 19
	s_add_u32 s0, s12, s0
	s_addc_u32 s1, s13, 0
	s_waitcnt lgkmcnt(0)
	s_barrier
	s_add_u32 s0, s0, 0x8100000
	s_addc_u32 s1, s1, 0
	v_cmp_gt_u32_e64 s[6:7], 32, v2
	v_cmp_lt_u32_e32 vcc, 31, v2
	s_and_saveexec_b64 s[10:11], vcc
	s_xor_b64 s[10:11], exec, s[10:11]
	s_lshl_b32 s14, s8, 8
	s_lshl_b32 s15, s17, 5
	s_or_saveexec_b64 s[10:11], s[10:11]
	v_mov_b32_e32 v216, s15
	v_mov_b32_e32 v215, s14
	s_xor_b64 exec, exec, s[10:11]
	s_cbranch_execz .LBB0_1327
	s_lshl_b32 s14, s17, 5
	v_or_b32_e32 v136, s14, v2
	v_lshl_add_u32 v132, v136, 4, 0
	ds_read_b128 v[132:135], v132
	s_lshl_b32 s8, s8, 8
	v_add_u32_e32 v136, s8, v136
	v_ashrrev_i32_e32 v137, 31, v136
	s_ashr_i32 s17, s16, 31
	s_waitcnt lgkmcnt(0)
	v_mov_b32_e32 v138, v133
	v_mov_b32_e32 v139, v134
	v_mov_b32_e32 v133, v135
	v_pk_add_f32 v[132:133], v[138:139], v[132:133]
	v_lshl_add_u64 v[134:135], v[136:137], 4, s[0:1]
	v_pk_add_f32 v[132:133], v[132:133], v[132:133] op_sel:[0,1] op_sel_hi:[1,0]
	v_lshl_add_u64 v[134:135], s[16:17], 2, v[134:135]
	v_add_u32_e32 v132, 1, v132
	v_mov_b32_e32 v216, s14
	v_mov_b32_e32 v215, s8
	global_store_dword v[134:135], v132, off sc1

; #define PG8_LAS __attribute__((address_space(3)))
;     __device__ __forceinline__ void publish(const f32x4 (&v)[2][2][4][2], const Unit& u, int wr, int wc, int fr, int fq, PG8_LAS unsigned char* lds, int wid, int lane) const {
;         PG8_LAS float* P = (PG8_LAS float*)lds;
; #pragma unroll
;         for (int ai = 0; ai < 2; ++ai)
; #pragma unroll
;             for (int m = 0; m < 4; ++m) {
;                 float s = 0.f;
; #pragma unroll
;                 for (int bj = 0; bj < 2; ++bj)
; #pragma unroll
;                     for (int n = 0; n < 2; ++n) { const f32x4 x = v[ai][bj][m][n]; s += (x[0] * x[0] + x[1] * x[1]) + (x[2] * x[2] + x[3] * x[3]); }
;                 s = xor_add<16>(s); s = xor_add<32>(s);
;                 if (fq == 0) P[(ai * HALF + wr * 64 + m * 16 + fr) * 4 + wc] = s;
;             }
;         asm volatile("s_waitcnt lgkmcnt(0)" ::: "memory"); __builtin_amdgcn_s_barrier(); asm volatile("" ::: "memory");
;         const int row = wid * 32 + (lane & 31);
;         if (lane < 32) {
;             const float tot = (P[row * 4 + 0] + P[row * 4 + 1]) + (P[row * 4 + 2] + P[row * 4 + 3]);
;             __hip_atomic_store(xbuf + ((size_t)(u.pm * BM + row) * 4 + u.pn), __float_as_uint(tot) + 1u, __ATOMIC_RELAXED, __HIP_MEMORY_SCOPE_AGENT);
;         }
.LBB0_1787:
	v_and_b32_e32 v2, 63, v146
	s_lshl_b32 s0, s25, 2
	v_cmp_gt_u32_e64 s[4:5], 16, v2
	s_add_i32 s18, s0, 0
	s_lshl_b32 s6, s22, 10
	s_add_i32 s6, s18, s6
	v_lshl_add_u32 v134, v147, 4, s6
	v_pk_mul_f32 v[244:245], v[116:117], v[116:117]
	v_pk_mul_f32 v[246:247], v[100:101], v[100:101]
	v_pk_fma_f32 v[244:245], v[118:119], v[118:119], v[244:245]
	v_pk_fma_f32 v[246:247], v[102:103], v[102:103], v[246:247]
	v_pk_fma_f32 v[244:245], v[120:121], v[120:121], v[244:245]
	v_pk_fma_f32 v[246:247], v[104:105], v[104:105], v[246:247]
	v_pk_fma_f32 v[244:245], v[122:123], v[122:123], v[244:245]
	v_pk_fma_f32 v[246:247], v[106:107], v[106:107], v[246:247]
	v_pk_fma_f32 v[244:245], v[124:125], v[124:125], v[244:245]
	v_pk_fma_f32 v[246:247], v[108:109], v[108:109], v[246:247]
	v_pk_fma_f32 v[244:245], v[126:127], v[126:127], v[244:245]
	v_pk_fma_f32 v[246:247], v[110:111], v[110:111], v[246:247]
	v_pk_fma_f32 v[244:245], v[128:129], v[128:129], v[244:245]
	v_pk_fma_f32 v[246:247], v[112:113], v[112:113], v[246:247]
	v_pk_fma_f32 v[244:245], v[130:131], v[130:131], v[244:245]
	v_pk_fma_f32 v[246:247], v[114:115], v[114:115], v[246:247]
	v_add_f32_e32 v236, v244, v245
	v_add_f32_e32 v237, v246, v247
	v_pk_mul_f32 v[244:245], v[84:85], v[84:85]
	v_pk_mul_f32 v[246:247], v[68:69], v[68:69]
	v_pk_fma_f32 v[244:245], v[86:87], v[86:87], v[244:245]
	v_pk_fma_f32 v[246:247], v[70:71], v[70:71], v[246:247]
	v_pk_fma_f32 v[244:245], v[88:89], v[88:89], v[244:245]
	v_pk_fma_f32 v[246:247], v[72:73], v[72:73], v[246:247]
	v_pk_fma_f32 v[244:245], v[90:91], v[90:91], v[244:245]
	v_pk_fma_f32 v[246:247], v[74:75], v[74:75], v[246:247]
	v_pk_fma_f32 v[244:245], v[92:93], v[92:93], v[244:245]
	v_pk_fma_f32 v[246:247], v[76:77], v[76:77], v[246:247]
	v_pk_fma_f32 v[244:245], v[94:95], v[94:95], v[244:245]
	v_pk_fma_f32 v[246:247], v[78:79], v[78:79], v[246:247]
	v_pk_fma_f32 v[244:245], v[96:97], v[96:97], v[244:245]
	v_pk_fma_f32 v[246:247], v[80:81], v[80:81], v[246:247]
	v_pk_fma_f32 v[244:245], v[98:99], v[98:99], v[244:245]
	v_pk_fma_f32 v[246:247], v[82:83], v[82:83], v[246:247]
	v_add_f32_e32 v238, v244, v245
	v_add_f32_e32 v239, v246, v247
	v_pk_mul_f32 v[244:245], v[52:53], v[52:53]
	v_pk_mul_f32 v[246:247], v[36:37], v[36:37]
	v_pk_fma_f32 v[244:245], v[54:55], v[54:55], v[244:245]
	v_pk_fma_f32 v[246:247], v[38:39], v[38:39], v[246:247]
	v_pk_fma_f32 v[244:245], v[56:57], v[56:57], v[244:245]
	v_pk_fma_f32 v[246:247], v[40:41], v[40:41], v[246:247]
	v_pk_fma_f32 v[244:245], v[58:59], v[58:59], v[244:245]
	v_pk_fma_f32 v[246:247], v[42:43], v[42:43], v[246:247]
	v_pk_fma_f32 v[244:245], v[60:61], v[60:61], v[244:245]
	v_pk_fma_f32 v[246:247], v[44:45], v[44:45], v[246:247]
	v_pk_fma_f32 v[244:245], v[62:63], v[62:63], v[244:245]
	v_pk_fma_f32 v[246:247], v[46:47], v[46:47], v[246:247]
	v_pk_fma_f32 v[244:245], v[64:65], v[64:65], v[244:245]
	v_pk_fma_f32 v[246:247], v[48:49], v[48:49], v[246:247]
	v_pk_fma_f32 v[244:245], v[66:67], v[66:67], v[244:245]
	v_pk_fma_f32 v[246:247], v[50:51], v[50:51], v[246:247]
	v_add_f32_e32 v240, v244, v245
	v_add_f32_e32 v241, v246, v247
	v_pk_mul_f32 v[244:245], v[20:21], v[20:21]
	v_pk_mul_f32 v[246:247], v[4:5], v[4:5]
	v_pk_fma_f32 v[244:245], v[22:23], v[22:23], v[244:245]
	v_pk_fma_f32 v[246:247], v[6:7], v[6:7], v[246:247]
	v_pk_fma_f32 v[244:245], v[24:25], v[24:25], v[244:245]
	v_pk_fma_f32 v[246:247], v[8:9], v[8:9], v[246:247]
	v_pk_fma_f32 v[244:245], v[26:27], v[26:27], v[244:245]
	v_pk_fma_f32 v[246:247], v[10:11], v[10:11], v[246:247]
	v_pk_fma_f32 v[244:245], v[28:29], v[28:29], v[244:245]
	v_pk_fma_f32 v[246:247], v[12:13], v[12:13], v[246:247]
	v_pk_fma_f32 v[244:245], v[30:31], v[30:31], v[244:245]
	v_pk_fma_f32 v[246:247], v[14:15], v[14:15], v[246:247]
	v_pk_fma_f32 v[244:245], v[32:33], v[32:33], v[244:245]
	v_pk_fma_f32 v[246:247], v[16:17], v[16:17], v[246:247]
	v_pk_fma_f32 v[244:245], v[34:35], v[34:35], v[244:245]
	v_pk_fma_f32 v[246:247], v[18:19], v[18:19], v[246:247]
	v_add_f32_e32 v242, v244, v245
	v_add_f32_e32 v243, v246, v247
	ds_swizzle_b32 v244, v236 offset:swizzle(SWAP,16)
	ds_swizzle_b32 v245, v237 offset:swizzle(SWAP,16)
	ds_swizzle_b32 v246, v238 offset:swizzle(SWAP,16)
	ds_swizzle_b32 v247, v239 offset:swizzle(SWAP,16)
	ds_swizzle_b32 v248, v240 offset:swizzle(SWAP,16)
	ds_swizzle_b32 v249, v241 offset:swizzle(SWAP,16)
	ds_swizzle_b32 v250, v242 offset:swizzle(SWAP,16)
	ds_swizzle_b32 v251, v243 offset:swizzle(SWAP,16)
	s_waitcnt lgkmcnt(0)
	v_add_f32_e32 v236, v236, v244
	v_add_f32_e32 v237, v237, v245
	v_add_f32_e32 v238, v238, v246
	v_add_f32_e32 v239, v239, v247
	v_add_f32_e32 v240, v240, v248
	v_add_f32_e32 v241, v241, v249
	v_add_f32_e32 v242, v242, v250
	v_add_f32_e32 v243, v243, v251
	v_mov_b32_e32 v244, v236
	v_mov_b32_e32 v245, v237
	v_mov_b32_e32 v246, v238
	v_mov_b32_e32 v247, v239
	v_mov_b32_e32 v248, v240
	v_mov_b32_e32 v249, v241
	v_mov_b32_e32 v250, v242
	v_mov_b32_e32 v251, v243
	s_nop 1
	v_permlane32_swap_b32_e32 v236, v244
	v_permlane32_swap_b32_e32 v237, v245
	v_permlane32_swap_b32_e32 v238, v246
	v_permlane32_swap_b32_e32 v239, v247
	v_permlane32_swap_b32_e32 v240, v248
	v_permlane32_swap_b32_e32 v241, v249
	v_permlane32_swap_b32_e32 v242, v250
	v_permlane32_swap_b32_e32 v243, v251
	s_barrier
	s_and_saveexec_b64 s[0:1], s[4:5]
	v_add_f32_e32 v236, v236, v244
	v_add_f32_e32 v237, v237, v245
	v_add_f32_e32 v238, v238, v246
	v_add_f32_e32 v239, v239, v247
	v_add_f32_e32 v240, v240, v248
	v_add_f32_e32 v241, v241, v249
	v_add_f32_e32 v242, v242, v250
	v_add_f32_e32 v243, v243, v251
	ds_write_b32 v134, v236
	ds_write_b32 v134, v237 offset:256
	ds_write_b32 v134, v238 offset:512
	ds_write_b32 v134, v239 offset:768
	ds_write_b32 v134, v240 offset:2048
	ds_write_b32 v134, v241 offset:2304
	ds_write_b32 v134, v242 offset:2560
	ds_write_b32 v134, v243 offset:2816
	s_or_b64 exec, exec, s[0:1]
	s_lshl_b32 s0, s77, 19
	s_add_u32 s0, s12, s0
	s_addc_u32 s1, s13, 0
	s_waitcnt lgkmcnt(0)
	s_barrier
	s_add_u32 s0, s0, 0x8140000
	s_addc_u32 s1, s1, 0
	v_cmp_gt_u32_e64 s[6:7], 32, v2
	v_cmp_lt_u32_e32 vcc, 31, v2
	s_and_saveexec_b64 s[8:9], vcc
	s_xor_b64 s[8:9], exec, s[8:9]
	s_lshl_b32 s10, s23, 8
	s_lshl_b32 s11, s17, 5
	s_or_saveexec_b64 s[8:9], s[8:9]
	v_mov_b32_e32 v230, s11
	v_mov_b32_e32 v229, s10
	s_xor_b64 exec, exec, s[8:9]
	s_cbranch_execz .LBB0_1807
	s_lshl_b32 s10, s17, 5
	v_or_b32_e32 v136, s10, v2
	v_lshl_add_u32 v132, v136, 4, 0
	ds_read_b128 v[132:135], v132
	s_lshl_b32 s11, s23, 8
	v_add_u32_e32 v136, s11, v136
	v_ashrrev_i32_e32 v137, 31, v136
	s_ashr_i32 s17, s16, 31
	s_waitcnt lgkmcnt(0)
	v_mov_b32_e32 v138, v133
	v_mov_b32_e32 v139, v134
	v_mov_b32_e32 v133, v135
	v_pk_add_f32 v[132:133], v[138:139], v[132:133]
	v_lshl_add_u64 v[134:135], v[136:137], 4, s[0:1]
	v_pk_add_f32 v[132:133], v[132:133], v[132:133] op_sel:[0,1] op_sel_hi:[1,0]
	v_lshl_add_u64 v[134:135], s[16:17], 2, v[134:135]
	v_add_u32_e32 v132, 1, v132
	v_mov_b32_e32 v230, s10
	v_mov_b32_e32 v229, s11
	global_store_dword v[134:135], v132, off sc1
